# nt cache policy on the combine phases' dwordx2 loads (fp8 expert-output gathers, read once)
# speedup vs baseline: 1.0074x; 1.0074x over previous
; __device__ __forceinline__ int tid_fresh() { int t = threadIdx.x; asm volatile("" : "+v"(t)); return t; }
; template <int MODE>
; __device__ __forceinline__ void combine_phase(LAS unsigned char* ldsb, int bid, int G, const float* x, const float* gf, const bf16_t* Y, const u32x2* rec,
;                                               float* xout, const float* ng, const float* sc, const float* sh, bf16_t* hbuf) {
;     ...
;     for (int rowi = bid * 16 + wave0 * 2; rowi < T; rowi += ((rowi & 1) ? (G * 16 - 1) : 1)) {
;         const int row = rowi;
;         const int lane = tid_fresh() & 63;
;         float a[4][8];
; #pragma unroll
;         for (int i = 0; i < 4; ++i)
; #pragma unroll
;             for (int q = 0; q < 8; ++q) a[i][q] = 0.f;
;         u32x2 rr[TOPK];
; #pragma unroll
;         for (int j = 0; j < TOPK; ++j) rr[j] = rec[row * TOPK + j];
;         float4 xr[4][2];
; #pragma unroll
;         for (int i = 0; i < 4; ++i) { const int c = lane * 8 + i * 512; xr[i][0] = *(const float4*)(x + (size_t)row * D + c); xr[i][1] = *(const float4*)(x + (size_t)row * D + c + 4); }
; #pragma unroll
;         for (int jb = 0; jb <= TOPK; jb += 8) {
;             u32x2 yv[7][4]; float wj[7];
; #pragma unroll
;             for (int jj = 0; jj < 7; ++jj) { const int j = jb + jj; if (j > TOPK) break;
;                 size_t slot = (size_t)SLOT_SH + row; wj[jj] = Y8_INV;
;                 if (j < TOPK) { const int e = (int)(rr[j].x >> 13), pos = (int)(rr[j].x & 8191u); wj[jj] = __uint_as_float(rr[j].y) * Y8_INV; slot = (size_t)tstart[e] * BM + pos; }
;                 const unsigned char* yp = (const unsigned char*)Y + slot * D + lane * 8;
; #pragma unroll
;                 for (int i = 0; i < 4; ++i) yv[jj][i] = *(const u32x2*)(yp + i * 512);
.LBB0_1221:
	v_mul_lo_u32 v2, v34, 6
	v_ashrrev_i32_e32 v3, 31, v2
	v_mov_b32_e32 v4, v0
	v_lshl_add_u64 v[2:3], v[2:3], 3, s[8:9]
	global_load_dwordx4 v[48:51], v[2:3], off
	global_load_dwordx4 v[52:55], v[2:3], off offset:16
	global_load_dwordx4 v[56:59], v[2:3], off offset:32
	v_and_b32_e32 v5, 1, v34
	v_cmp_eq_u32_e32 vcc, 1, v5
	v_lshlrev_b32_e32 v11, 3, v4
	v_ashrrev_i32_e32 v35, 31, v34
	v_cndmask_b32_e32 v10, 1, v1, vcc
	v_and_b32_e32 v36, 0x1f8, v11
	v_lshlrev_b64 v[6:7], 13, v[34:35]
	v_lshlrev_b64 v[8:9], 11, v[34:35]
	v_add_u32_e32 v34, v10, v34
	v_lshl_add_u64 v[86:87], s[6:7], 0, v[36:37]
	v_cmp_lt_i32_e32 vcc, s16, v34
	v_lshlrev_b32_e32 v40, 2, v36
	v_lshl_add_u64 v[2:3], v[86:87], 0, v[8:9]
	v_mov_b32_e32 v41, v37
	v_mov_b32_e32 v39, v37
	v_lshl_add_u64 v[4:5], s[68:69], 0, v[6:7]
	s_or_b64 s[2:3], vcc, s[2:3]
	v_or_b32_e32 v38, 0x1000, v40
	v_add_co_u32_e32 v64, vcc, s15, v2
	v_mov_b32_e32 v43, v37
	v_lshl_add_u64 v[6:7], s[10:11], 0, v[6:7]
	v_lshl_add_u64 v[14:15], v[4:5], 0, v[40:41]
	v_or_b32_e32 v42, 0x1800, v40
	v_lshl_add_u64 v[60:61], v[4:5], 0, v[38:39]
	v_addc_co_u32_e32 v65, vcc, 0, v3, vcc
	v_lshl_add_u64 v[44:45], v[6:7], 0, v[40:41]
	v_lshl_add_u64 v[62:63], v[4:5], 0, v[42:43]
	global_load_dwordx4 v[6:9], v[14:15], off offset:16
	global_load_dwordx4 v[18:21], v[14:15], off
	global_load_dwordx4 v[2:5], v[14:15], off offset:2064
	global_load_dwordx4 v[10:13], v[14:15], off offset:2048
	global_load_dwordx2 v[66:67], v[64:65], off nt
	global_load_dwordx2 v[68:69], v[64:65], off offset:512 nt
	global_load_dwordx2 v[74:75], v[64:65], off offset:1024 nt
	global_load_dwordx2 v[82:83], v[64:65], off offset:1536 nt
	global_load_dwordx4 v[22:25], v[60:61], off offset:16
	global_load_dwordx4 v[30:33], v[60:61], off
	global_load_dwordx4 v[14:17], v[62:63], off offset:16
	global_load_dwordx4 v[26:29], v[62:63], off
	v_or_b32_e32 v35, 0x800, v40
	v_add_co_u32_e32 v46, vcc, s13, v44
	s_waitcnt vmcnt(14)
	v_lshrrev_b32_e32 v36, 11, v48
	v_lshlrev_b32_e32 v39, 11, v48
	v_lshrrev_b32_e32 v41, 11, v50
	s_waitcnt vmcnt(13)
	v_lshrrev_b32_e32 v60, 11, v52
	v_lshlrev_b32_e32 v85, 11, v52
	v_lshrrev_b32_e32 v52, 11, v54
	v_lshlrev_b32_e32 v100, 11, v54
	s_waitcnt vmcnt(12)
	v_lshrrev_b32_e32 v54, 11, v56
	v_lshlrev_b32_e32 v101, 11, v56
	v_lshrrev_b32_e32 v56, 11, v58
	v_mul_f32_e32 v116, 0x3d800000, v51
	v_and_b32_e32 v51, 0x1ffffc, v36
	v_mul_f32_e32 v118, 0x3d800000, v53
	v_and_b32_e32 v36, 0xfff800, v39
	v_and_b32_e32 v39, 0x1ffffc, v41
	v_and_b32_e32 v41, 0x1ffffc, v60
	v_and_b32_e32 v52, 0x1ffffc, v52
	v_and_b32_e32 v53, 0x1ffffc, v54
	v_and_b32_e32 v54, 0x1ffffc, v56
	v_add_u32_e32 v51, s14, v51
	v_add_u32_e32 v39, s14, v39
	v_add_u32_e32 v41, s14, v41
	v_add_u32_e32 v52, s14, v52
	v_add_u32_e32 v53, s14, v53
	v_add_u32_e32 v54, s14, v54
	ds_read_b32 v88, v51
	ds_read_b32 v90, v39
	ds_read_b32 v92, v41
	ds_read_b32 v94, v52
	ds_read_b32 v96, v53
	ds_read_b32 v98, v54
	s_waitcnt lgkmcnt(5)
	v_ashrrev_i32_e32 v89, 31, v88
	s_waitcnt lgkmcnt(4)
	v_ashrrev_i32_e32 v91, 31, v90
	v_lshlrev_b64 v[88:89], 19, v[88:89]
	v_lshlrev_b32_e32 v43, 11, v50
	v_lshlrev_b64 v[90:91], 19, v[90:91]
	v_lshl_add_u64 v[88:89], v[86:87], 0, v[88:89]
	s_waitcnt lgkmcnt(3)
	v_ashrrev_i32_e32 v93, 31, v92
	v_lshl_add_u64 v[90:91], v[86:87], 0, v[90:91]
	v_lshl_add_u64 v[88:89], v[88:89], 0, v[36:37]
	v_and_b32_e32 v36, 0xfff800, v43
	s_waitcnt lgkmcnt(2)
	v_ashrrev_i32_e32 v95, 31, v94
	v_lshlrev_b64 v[92:93], 19, v[92:93]
	global_load_dwordx2 v[120:121], v[88:89], off nt
	global_load_dwordx2 v[122:123], v[88:89], off offset:512 nt
	global_load_dwordx2 v[124:125], v[88:89], off offset:1024 nt
	global_load_dwordx2 v[126:127], v[88:89], off offset:1536 nt
	v_lshl_add_u64 v[88:89], v[90:91], 0, v[36:37]
	s_waitcnt lgkmcnt(1)
	v_ashrrev_i32_e32 v97, 31, v96
	v_lshlrev_b64 v[94:95], 19, v[94:95]
	v_lshl_add_u64 v[92:93], v[86:87], 0, v[92:93]
	v_and_b32_e32 v36, 0xfff800, v85
	global_load_dwordx2 v[128:129], v[88:89], off nt
	global_load_dwordx2 v[130:131], v[88:89], off offset:512 nt
	global_load_dwordx2 v[132:133], v[88:89], off offset:1024 nt
	global_load_dwordx2 v[134:135], v[88:89], off offset:1536 nt
	s_waitcnt lgkmcnt(0)
	v_ashrrev_i32_e32 v99, 31, v98
	v_lshlrev_b64 v[96:97], 19, v[96:97]
	v_lshl_add_u64 v[94:95], v[86:87], 0, v[94:95]
	v_lshl_add_u64 v[88:89], v[92:93], 0, v[36:37]
	v_and_b32_e32 v36, 0xfff800, v100
	v_mul_f32_e32 v114, 0x3d800000, v49
	v_lshlrev_b32_e32 v49, 11, v58
	v_lshlrev_b64 v[98:99], 19, v[98:99]
	v_lshl_add_u64 v[96:97], v[86:87], 0, v[96:97]
	global_load_dwordx2 v[136:137], v[88:89], off nt
	global_load_dwordx2 v[138:139], v[88:89], off offset:512 nt
	global_load_dwordx2 v[140:141], v[88:89], off offset:1024 nt
	global_load_dwordx2 v[142:143], v[88:89], off offset:1536 nt
	v_lshl_add_u64 v[88:89], v[94:95], 0, v[36:37]
	v_and_b32_e32 v36, 0xfff800, v101
	v_lshl_add_u64 v[86:87], v[86:87], 0, v[98:99]
	global_load_dwordx2 v[144:145], v[88:89], off nt
	global_load_dwordx2 v[146:147], v[88:89], off offset:512 nt
	global_load_dwordx2 v[148:149], v[88:89], off offset:1024 nt
	global_load_dwordx2 v[150:151], v[88:89], off offset:1536 nt
	v_lshl_add_u64 v[88:89], v[96:97], 0, v[36:37]
	v_and_b32_e32 v36, 0xfff800, v49
	global_load_dwordx2 v[152:153], v[88:89], off nt
	global_load_dwordx2 v[154:155], v[88:89], off offset:512 nt
	global_load_dwordx2 v[156:157], v[88:89], off offset:1024 nt
	global_load_dwordx2 v[158:159], v[88:89], off offset:1536 nt
	v_lshl_add_u64 v[86:87], v[86:87], 0, v[36:37]
	global_load_dwordx2 v[160:161], v[86:87], off nt
	global_load_dwordx2 v[162:163], v[86:87], off offset:512 nt
	global_load_dwordx2 v[164:165], v[86:87], off offset:1024 nt
	global_load_dwordx2 v[166:167], v[86:87], off offset:1536 nt
	global_load_dwordx4 v[86:89], v40, s[4:5] offset:16
	global_load_dwordx4 v[90:93], v40, s[4:5]
	global_load_dwordx4 v[94:97], v35, s[4:5] offset:16
	global_load_dwordx4 v[98:101], v35, s[4:5]
	global_load_dwordx4 v[102:105], v38, s[4:5] offset:16
	s_nop 0
	global_load_dwordx4 v[38:41], v38, s[4:5]
	s_nop 0
	global_load_dwordx4 v[106:109], v42, s[4:5] offset:16
	global_load_dwordx4 v[110:113], v42, s[4:5]
	v_mul_f32_e32 v84, 0x3d800000, v55
	s_waitcnt vmcnt(39)
; template <int MODE>
; __device__ __forceinline__ void combine_phase(LAS unsigned char* ldsb, int bid, int G, const float* x, const float* gf, const bf16_t* Y, const u32x2* rec,
;                                               float* xout, const float* ng, const float* sc, const float* sh, bf16_t* hbuf) {
;     ...
;             for (int jj = 0; jj < 7; ++jj) { const int j = jb + jj; if (j > TOPK) break; const float w = wj[jj];
; #pragma unroll
;                 for (int i = 0; i < 4; ++i) { const u32x2 y2 = yv[jj][i];
;                     const f32x2v p0 = __builtin_amdgcn_cvt_pk_f32_fp8((int)y2.x, false), p1 = __builtin_amdgcn_cvt_pk_f32_fp8((int)y2.x, true), p2 = __builtin_amdgcn_cvt_pk_f32_fp8((int)y2.y, false), p3 = __builtin_amdgcn_cvt_pk_f32_fp8((int)y2.y, true);
;                     a[i][0] += w * p0.x; a[i][1] += w * p0.y; a[i][2] += w * p1.x; a[i][3] += w * p1.y;
;                     a[i][4] += w * p2.x; a[i][5] += w * p2.y; a[i][6] += w * p3.x; a[i][7] += w * p3.y; }
;             }
	v_cvt_pk_f32_fp8_e32 v[52:53], v66
	v_cvt_pk_f32_fp8_sdwa v[54:55], v66 src0_sel:WORD_1
	v_mul_f32_e32 v50, 0x3d800000, v57
	v_mul_f32_e32 v48, 0x3d800000, v59
	v_cvt_pk_f32_fp8_e32 v[56:57], v67
	v_cvt_pk_f32_fp8_sdwa v[58:59], v67 src0_sel:WORD_1
	s_waitcnt vmcnt(38)
	v_cvt_pk_f32_fp8_e32 v[60:61], v68
	v_cvt_pk_f32_fp8_sdwa v[62:63], v68 src0_sel:WORD_1
	v_cvt_pk_f32_fp8_e32 v[64:65], v69
	v_cvt_pk_f32_fp8_sdwa v[66:67], v69 src0_sel:WORD_1
	s_waitcnt vmcnt(37)
	v_cvt_pk_f32_fp8_e32 v[68:69], v74
	v_cvt_pk_f32_fp8_sdwa v[70:71], v74 src0_sel:WORD_1
	v_cvt_pk_f32_fp8_e32 v[72:73], v75
	v_cvt_pk_f32_fp8_sdwa v[74:75], v75 src0_sel:WORD_1
	s_waitcnt vmcnt(36)
	v_cvt_pk_f32_fp8_e32 v[76:77], v82
	v_cvt_pk_f32_fp8_sdwa v[78:79], v82 src0_sel:WORD_1
	v_cvt_pk_f32_fp8_e32 v[80:81], v83
	v_cvt_pk_f32_fp8_sdwa v[82:83], v83 src0_sel:WORD_1
	v_addc_co_u32_e32 v47, vcc, 0, v45, vcc
	s_waitcnt vmcnt(31)
	v_cvt_pk_f32_fp8_e32 v[42:43], v120
	v_cvt_pk_f32_fp8_sdwa v[168:169], v120 src0_sel:WORD_1
	v_cvt_pk_f32_fp8_e32 v[170:171], v121
	v_cvt_pk_f32_fp8_sdwa v[120:121], v121 src0_sel:WORD_1
	s_waitcnt vmcnt(30)
	v_cvt_pk_f32_fp8_e32 v[172:173], v122
	v_cvt_pk_f32_fp8_sdwa v[174:175], v122 src0_sel:WORD_1
	v_cvt_pk_f32_fp8_e32 v[176:177], v123
	v_cvt_pk_f32_fp8_sdwa v[122:123], v123 src0_sel:WORD_1
	s_waitcnt vmcnt(29)
	v_cvt_pk_f32_fp8_e32 v[178:179], v124
	v_cvt_pk_f32_fp8_sdwa v[180:181], v124 src0_sel:WORD_1
	v_cvt_pk_f32_fp8_e32 v[182:183], v125
	v_cvt_pk_f32_fp8_sdwa v[124:125], v125 src0_sel:WORD_1
	s_waitcnt vmcnt(28)
	v_cvt_pk_f32_fp8_e32 v[184:185], v126
	v_cvt_pk_f32_fp8_sdwa v[186:187], v126 src0_sel:WORD_1
	v_cvt_pk_f32_fp8_e32 v[188:189], v127
	v_cvt_pk_f32_fp8_sdwa v[126:127], v127 src0_sel:WORD_1
	s_waitcnt vmcnt(27)
	v_cvt_pk_f32_fp8_e32 v[190:191], v128
	v_cvt_pk_f32_fp8_sdwa v[192:193], v128 src0_sel:WORD_1
	v_cvt_pk_f32_fp8_e32 v[194:195], v129
	v_cvt_pk_f32_fp8_sdwa v[128:129], v129 src0_sel:WORD_1
	s_waitcnt vmcnt(26)
	v_cvt_pk_f32_fp8_e32 v[196:197], v130
	v_cvt_pk_f32_fp8_sdwa v[198:199], v130 src0_sel:WORD_1
	v_cvt_pk_f32_fp8_e32 v[200:201], v131
	v_cvt_pk_f32_fp8_sdwa v[130:131], v131 src0_sel:WORD_1
	s_waitcnt vmcnt(25)
	v_cvt_pk_f32_fp8_e32 v[202:203], v132
	v_cvt_pk_f32_fp8_sdwa v[204:205], v132 src0_sel:WORD_1
	v_cvt_pk_f32_fp8_e32 v[206:207], v133
	v_cvt_pk_f32_fp8_sdwa v[132:133], v133 src0_sel:WORD_1
	s_waitcnt vmcnt(24)
	v_cvt_pk_f32_fp8_e32 v[208:209], v134
	v_cvt_pk_f32_fp8_sdwa v[210:211], v134 src0_sel:WORD_1
	v_cvt_pk_f32_fp8_e32 v[212:213], v135
	v_cvt_pk_f32_fp8_sdwa v[134:135], v135 src0_sel:WORD_1
	s_waitcnt vmcnt(23)
	v_cvt_pk_f32_fp8_e32 v[214:215], v136
	v_cvt_pk_f32_fp8_sdwa v[216:217], v136 src0_sel:WORD_1
	v_cvt_pk_f32_fp8_e32 v[218:219], v137
	v_cvt_pk_f32_fp8_sdwa v[136:137], v137 src0_sel:WORD_1
	s_waitcnt vmcnt(22)
	v_cvt_pk_f32_fp8_e32 v[220:221], v138
	v_cvt_pk_f32_fp8_sdwa v[222:223], v138 src0_sel:WORD_1
	v_cvt_pk_f32_fp8_e32 v[224:225], v139
	v_cvt_pk_f32_fp8_sdwa v[138:139], v139 src0_sel:WORD_1
	s_waitcnt vmcnt(21)
	v_cvt_pk_f32_fp8_e32 v[226:227], v140
	v_cvt_pk_f32_fp8_sdwa v[228:229], v140 src0_sel:WORD_1
	v_cvt_pk_f32_fp8_e32 v[230:231], v141
	v_cvt_pk_f32_fp8_sdwa v[140:141], v141 src0_sel:WORD_1
	s_waitcnt vmcnt(20)
	v_cvt_pk_f32_fp8_e32 v[232:233], v142
	v_cvt_pk_f32_fp8_sdwa v[234:235], v142 src0_sel:WORD_1
	v_cvt_pk_f32_fp8_e32 v[236:237], v143
	v_cvt_pk_f32_fp8_sdwa v[142:143], v143 src0_sel:WORD_1
	s_waitcnt vmcnt(19)
	v_cvt_pk_f32_fp8_e32 v[238:239], v144
	v_cvt_pk_f32_fp8_sdwa v[240:241], v144 src0_sel:WORD_1
	v_pk_fma_f32 v[42:43], v[114:115], v[42:43], 0 op_sel_hi:[0,1,0]
	v_pk_fma_f32 v[168:169], v[114:115], v[168:169], 0 op_sel_hi:[0,1,0]
	v_pk_fma_f32 v[170:171], v[114:115], v[170:171], 0 op_sel_hi:[0,1,0]
	v_pk_fma_f32 v[120:121], v[114:115], v[120:121], 0 op_sel_hi:[0,1,0]
	v_pk_fma_f32 v[172:173], v[114:115], v[172:173], 0 op_sel_hi:[0,1,0]
	v_pk_fma_f32 v[174:175], v[114:115], v[174:175], 0 op_sel_hi:[0,1,0]
	v_cvt_pk_f32_fp8_e32 v[242:243], v145
	v_cvt_pk_f32_fp8_sdwa v[144:145], v145 src0_sel:WORD_1
	s_waitcnt vmcnt(18)
	v_cvt_pk_f32_fp8_e32 v[244:245], v146
	v_cvt_pk_f32_fp8_sdwa v[246:247], v146 src0_sel:WORD_1
	v_cvt_pk_f32_fp8_e32 v[248:249], v147
	v_cvt_pk_f32_fp8_sdwa v[146:147], v147 src0_sel:WORD_1
	s_waitcnt vmcnt(17)
	v_cvt_pk_f32_fp8_e32 v[250:251], v148
	v_pk_fma_f32 v[176:177], v[114:115], v[176:177], 0 op_sel_hi:[0,1,0]
	v_pk_fma_f32 v[122:123], v[114:115], v[122:123], 0 op_sel_hi:[0,1,0]
	v_pk_fma_f32 v[178:179], v[114:115], v[178:179], 0 op_sel_hi:[0,1,0]
	v_pk_fma_f32 v[180:181], v[114:115], v[180:181], 0 op_sel_hi:[0,1,0]
	v_pk_fma_f32 v[182:183], v[114:115], v[182:183], 0 op_sel_hi:[0,1,0]
	v_pk_fma_f32 v[124:125], v[114:115], v[124:125], 0 op_sel_hi:[0,1,0]
	v_pk_fma_f32 v[184:185], v[114:115], v[184:185], 0 op_sel_hi:[0,1,0]
	v_pk_fma_f32 v[186:187], v[114:115], v[186:187], 0 op_sel_hi:[0,1,0]
	v_pk_fma_f32 v[188:189], v[114:115], v[188:189], 0 op_sel_hi:[0,1,0]
	v_pk_fma_f32 v[114:115], v[114:115], v[126:127], 0 op_sel_hi:[0,1,0]
	v_cvt_pk_f32_fp8_sdwa v[126:127], v148 src0_sel:WORD_1
	v_pk_fma_f32 v[42:43], v[116:117], v[190:191], v[42:43] op_sel_hi:[0,1,1]
	v_cvt_pk_f32_fp8_e32 v[190:191], v149
	v_cvt_pk_f32_fp8_sdwa v[148:149], v149 src0_sel:WORD_1
	v_pk_fma_f32 v[168:169], v[116:117], v[192:193], v[168:169] op_sel_hi:[0,1,1]
	s_waitcnt vmcnt(16)
	v_cvt_pk_f32_fp8_e32 v[192:193], v150
	v_pk_fma_f32 v[170:171], v[116:117], v[194:195], v[170:171] op_sel_hi:[0,1,1]
	v_cvt_pk_f32_fp8_sdwa v[194:195], v150 src0_sel:WORD_1
	v_pk_fma_f32 v[120:121], v[116:117], v[128:129], v[120:121] op_sel_hi:[0,1,1]
	v_cvt_pk_f32_fp8_e32 v[128:129], v151
	v_cvt_pk_f32_fp8_sdwa v[150:151], v151 src0_sel:WORD_1
	v_pk_fma_f32 v[172:173], v[116:117], v[196:197], v[172:173] op_sel_hi:[0,1,1]
	s_waitcnt vmcnt(15)
; template <int MODE>
; __device__ __forceinline__ void combine_phase(LAS unsigned char* ldsb, int bid, int G, const float* x, const float* gf, const bf16_t* Y, const u32x2* rec,
;                                               float* xout, const float* ng, const float* sc, const float* sh, bf16_t* hbuf) {
;     ...
;             for (int jj = 0; jj < 7; ++jj) { const int j = jb + jj; if (j > TOPK) break; const float w = wj[jj];
; #pragma unroll
;                 for (int i = 0; i < 4; ++i) { const u32x2 y2 = yv[jj][i];
;                     const f32x2v p0 = __builtin_amdgcn_cvt_pk_f32_fp8((int)y2.x, false), p1 = __builtin_amdgcn_cvt_pk_f32_fp8((int)y2.x, true), p2 = __builtin_amdgcn_cvt_pk_f32_fp8((int)y2.y, false), p3 = __builtin_amdgcn_cvt_pk_f32_fp8((int)y2.y, true);
;                     a[i][0] += w * p0.x; a[i][1] += w * p0.y; a[i][2] += w * p1.x; a[i][3] += w * p1.y;
;                     a[i][4] += w * p2.x; a[i][5] += w * p2.y; a[i][6] += w * p3.x; a[i][7] += w * p3.y; }
;             }
	v_cvt_pk_f32_fp8_e32 v[196:197], v152
	v_pk_fma_f32 v[174:175], v[116:117], v[198:199], v[174:175] op_sel_hi:[0,1,1]
	v_cvt_pk_f32_fp8_sdwa v[198:199], v152 src0_sel:WORD_1
	v_pk_fma_f32 v[176:177], v[116:117], v[200:201], v[176:177] op_sel_hi:[0,1,1]
	v_cvt_pk_f32_fp8_e32 v[200:201], v153
	v_cvt_pk_f32_fp8_sdwa v[152:153], v153 src0_sel:WORD_1
	v_pk_fma_f32 v[122:123], v[116:117], v[130:131], v[122:123] op_sel_hi:[0,1,1]
	s_waitcnt vmcnt(14)
	v_cvt_pk_f32_fp8_e32 v[130:131], v154
	v_pk_fma_f32 v[178:179], v[116:117], v[202:203], v[178:179] op_sel_hi:[0,1,1]
	v_cvt_pk_f32_fp8_sdwa v[202:203], v154 src0_sel:WORD_1
	v_pk_fma_f32 v[180:181], v[116:117], v[204:205], v[180:181] op_sel_hi:[0,1,1]
	v_cvt_pk_f32_fp8_e32 v[204:205], v155
	v_cvt_pk_f32_fp8_sdwa v[154:155], v155 src0_sel:WORD_1
	v_pk_fma_f32 v[182:183], v[116:117], v[206:207], v[182:183] op_sel_hi:[0,1,1]
	s_waitcnt vmcnt(13)
	v_cvt_pk_f32_fp8_e32 v[206:207], v156
	v_pk_fma_f32 v[124:125], v[116:117], v[132:133], v[124:125] op_sel_hi:[0,1,1]
	v_cvt_pk_f32_fp8_sdwa v[132:133], v156 src0_sel:WORD_1
	v_pk_fma_f32 v[184:185], v[116:117], v[208:209], v[184:185] op_sel_hi:[0,1,1]
	v_cvt_pk_f32_fp8_e32 v[208:209], v157
	v_cvt_pk_f32_fp8_sdwa v[156:157], v157 src0_sel:WORD_1
	v_pk_fma_f32 v[186:187], v[116:117], v[210:211], v[186:187] op_sel_hi:[0,1,1]
	s_waitcnt vmcnt(12)
	v_cvt_pk_f32_fp8_e32 v[210:211], v158
	v_pk_fma_f32 v[188:189], v[116:117], v[212:213], v[188:189] op_sel_hi:[0,1,1]
	v_cvt_pk_f32_fp8_sdwa v[212:213], v158 src0_sel:WORD_1
	v_pk_fma_f32 v[114:115], v[116:117], v[134:135], v[114:115] op_sel_hi:[0,1,1]
	v_cvt_pk_f32_fp8_e32 v[116:117], v159
	v_cvt_pk_f32_fp8_sdwa v[134:135], v159 src0_sel:WORD_1
	s_waitcnt vmcnt(11)
	v_cvt_pk_f32_fp8_e32 v[158:159], v160
	v_pk_fma_f32 v[42:43], v[118:119], v[214:215], v[42:43] op_sel_hi:[0,1,1]
	v_cvt_pk_f32_fp8_sdwa v[214:215], v160 src0_sel:WORD_1
	v_pk_fma_f32 v[168:169], v[118:119], v[216:217], v[168:169] op_sel_hi:[0,1,1]
	v_cvt_pk_f32_fp8_e32 v[216:217], v161
	v_cvt_pk_f32_fp8_sdwa v[160:161], v161 src0_sel:WORD_1
	v_pk_fma_f32 v[170:171], v[118:119], v[218:219], v[170:171] op_sel_hi:[0,1,1]
	s_waitcnt vmcnt(10)
	v_cvt_pk_f32_fp8_e32 v[218:219], v162
	v_pk_fma_f32 v[120:121], v[118:119], v[136:137], v[120:121] op_sel_hi:[0,1,1]
	v_cvt_pk_f32_fp8_sdwa v[136:137], v162 src0_sel:WORD_1
	v_pk_fma_f32 v[172:173], v[118:119], v[220:221], v[172:173] op_sel_hi:[0,1,1]
	v_cvt_pk_f32_fp8_e32 v[220:221], v163
	v_cvt_pk_f32_fp8_sdwa v[162:163], v163 src0_sel:WORD_1
	v_pk_fma_f32 v[174:175], v[118:119], v[222:223], v[174:175] op_sel_hi:[0,1,1]
	s_waitcnt vmcnt(9)
	v_cvt_pk_f32_fp8_e32 v[222:223], v164
	v_pk_fma_f32 v[176:177], v[118:119], v[224:225], v[176:177] op_sel_hi:[0,1,1]
	v_cvt_pk_f32_fp8_sdwa v[224:225], v164 src0_sel:WORD_1
	v_pk_fma_f32 v[122:123], v[118:119], v[138:139], v[122:123] op_sel_hi:[0,1,1]
	v_cvt_pk_f32_fp8_e32 v[138:139], v165
	v_cvt_pk_f32_fp8_sdwa v[164:165], v165 src0_sel:WORD_1
	v_pk_fma_f32 v[178:179], v[118:119], v[226:227], v[178:179] op_sel_hi:[0,1,1]
	s_waitcnt vmcnt(8)
; template <int MODE>
; __device__ __forceinline__ void combine_phase(LAS unsigned char* ldsb, int bid, int G, const float* x, const float* gf, const bf16_t* Y, const u32x2* rec,
;                                               float* xout, const float* ng, const float* sc, const float* sh, bf16_t* hbuf) {
;     ...
;             for (int jj = 0; jj < 7; ++jj) { const int j = jb + jj; if (j > TOPK) break; const float w = wj[jj];
; #pragma unroll
;                 for (int i = 0; i < 4; ++i) { const u32x2 y2 = yv[jj][i];
;                     const f32x2v p0 = __builtin_amdgcn_cvt_pk_f32_fp8((int)y2.x, false), p1 = __builtin_amdgcn_cvt_pk_f32_fp8((int)y2.x, true), p2 = __builtin_amdgcn_cvt_pk_f32_fp8((int)y2.y, false), p3 = __builtin_amdgcn_cvt_pk_f32_fp8((int)y2.y, true);
;                     a[i][0] += w * p0.x; a[i][1] += w * p0.y; a[i][2] += w * p1.x; a[i][3] += w * p1.y;
;                     a[i][4] += w * p2.x; a[i][5] += w * p2.y; a[i][6] += w * p3.x; a[i][7] += w * p3.y; }
;             }
;             asm volatile("" ::: "memory");
;         }
;         float ss = 0.f;
; #pragma unroll
;         for (int i = 0; i < 4; ++i) { const int c = lane * 8 + i * 512;
; #pragma unroll
;             for (int h = 0; h < 2; ++h) { const float4 xv = xr[i][h], gv = *(const float4*)(gf + c + h * 4);
;                 a[i][h * 4 + 0] = xv.x + gv.x * a[i][h * 4 + 0]; a[i][h * 4 + 1] = xv.y + gv.y * a[i][h * 4 + 1]; a[i][h * 4 + 2] = xv.z + gv.z * a[i][h * 4 + 2]; a[i][h * 4 + 3] = xv.w + gv.w * a[i][h * 4 + 3]; }
; #pragma unroll
;             for (int q = 0; q < 8; ++q) ss += a[i][q] * a[i][q]; }
;         if (MODE == 0 || MODE == 2) {
; #pragma unroll
;             for (int i = 0; i < 4; ++i) { float* op = xout + (size_t)row * D + lane * 8 + i * 512; *(float4*)op = make_float4(a[i][0], a[i][1], a[i][2], a[i][3]); *(float4*)(op + 4) = make_float4(a[i][4], a[i][5], a[i][6], a[i][7]); }
	v_cvt_pk_f32_fp8_e32 v[226:227], v166
	v_pk_fma_f32 v[180:181], v[118:119], v[228:229], v[180:181] op_sel_hi:[0,1,1]
	v_cvt_pk_f32_fp8_sdwa v[228:229], v166 src0_sel:WORD_1
	v_pk_fma_f32 v[182:183], v[118:119], v[230:231], v[182:183] op_sel_hi:[0,1,1]
	v_cvt_pk_f32_fp8_e32 v[230:231], v167
	v_cvt_pk_f32_fp8_sdwa v[166:167], v167 src0_sel:WORD_1
	v_pk_fma_f32 v[124:125], v[118:119], v[140:141], v[124:125] op_sel_hi:[0,1,1]
	v_pk_fma_f32 v[140:141], v[118:119], v[232:233], v[184:185] op_sel_hi:[0,1,1]
	v_pk_fma_f32 v[184:185], v[118:119], v[234:235], v[186:187] op_sel_hi:[0,1,1]
	v_pk_fma_f32 v[186:187], v[118:119], v[236:237], v[188:189] op_sel_hi:[0,1,1]
	v_pk_fma_f32 v[114:115], v[118:119], v[142:143], v[114:115] op_sel_hi:[0,1,1]
	v_pk_fma_f32 v[42:43], v[84:85], v[238:239], v[42:43] op_sel_hi:[0,1,1]
	v_pk_fma_f32 v[118:119], v[84:85], v[240:241], v[168:169] op_sel_hi:[0,1,1]
	v_pk_fma_f32 v[142:143], v[84:85], v[242:243], v[170:171] op_sel_hi:[0,1,1]
	v_pk_fma_f32 v[120:121], v[84:85], v[144:145], v[120:121] op_sel_hi:[0,1,1]
	v_pk_fma_f32 v[144:145], v[84:85], v[244:245], v[172:173] op_sel_hi:[0,1,1]
	v_pk_fma_f32 v[168:169], v[84:85], v[246:247], v[174:175] op_sel_hi:[0,1,1]
	v_pk_fma_f32 v[170:171], v[84:85], v[248:249], v[176:177] op_sel_hi:[0,1,1]
	v_pk_fma_f32 v[122:123], v[84:85], v[146:147], v[122:123] op_sel_hi:[0,1,1]
	v_pk_fma_f32 v[146:147], v[84:85], v[250:251], v[178:179] op_sel_hi:[0,1,1]
	v_pk_fma_f32 v[126:127], v[84:85], v[126:127], v[180:181] op_sel_hi:[0,1,1]
	v_pk_fma_f32 v[172:173], v[84:85], v[190:191], v[182:183] op_sel_hi:[0,1,1]
	v_pk_fma_f32 v[124:125], v[84:85], v[148:149], v[124:125] op_sel_hi:[0,1,1]
	v_pk_fma_f32 v[140:141], v[84:85], v[192:193], v[140:141] op_sel_hi:[0,1,1]
	v_pk_fma_f32 v[148:149], v[84:85], v[194:195], v[184:185] op_sel_hi:[0,1,1]
	v_pk_fma_f32 v[128:129], v[84:85], v[128:129], v[186:187] op_sel_hi:[0,1,1]
	v_pk_fma_f32 v[84:85], v[84:85], v[150:151], v[114:115] op_sel_hi:[0,1,1]
	v_pk_fma_f32 v[42:43], v[50:51], v[196:197], v[42:43] op_sel_hi:[0,1,1]
	v_pk_fma_f32 v[114:115], v[50:51], v[198:199], v[118:119] op_sel_hi:[0,1,1]
	v_pk_fma_f32 v[118:119], v[50:51], v[200:201], v[142:143] op_sel_hi:[0,1,1]
	v_pk_fma_f32 v[120:121], v[50:51], v[152:153], v[120:121] op_sel_hi:[0,1,1]
	v_pk_fma_f32 v[130:131], v[50:51], v[130:131], v[144:145] op_sel_hi:[0,1,1]
	v_pk_fma_f32 v[142:143], v[50:51], v[202:203], v[168:169] op_sel_hi:[0,1,1]
	v_pk_fma_f32 v[144:145], v[50:51], v[204:205], v[170:171] op_sel_hi:[0,1,1]
	v_pk_fma_f32 v[122:123], v[50:51], v[154:155], v[122:123] op_sel_hi:[0,1,1]
	v_pk_fma_f32 v[146:147], v[50:51], v[206:207], v[146:147] op_sel_hi:[0,1,1]
	v_pk_fma_f32 v[126:127], v[50:51], v[132:133], v[126:127] op_sel_hi:[0,1,1]
	v_pk_fma_f32 v[132:133], v[50:51], v[208:209], v[172:173] op_sel_hi:[0,1,1]
	v_pk_fma_f32 v[124:125], v[50:51], v[156:157], v[124:125] op_sel_hi:[0,1,1]
	v_pk_fma_f32 v[140:141], v[50:51], v[210:211], v[140:141] op_sel_hi:[0,1,1]
	v_pk_fma_f32 v[148:149], v[50:51], v[212:213], v[148:149] op_sel_hi:[0,1,1]
	v_pk_fma_f32 v[116:117], v[50:51], v[116:117], v[128:129] op_sel_hi:[0,1,1]
	v_pk_fma_f32 v[50:51], v[50:51], v[134:135], v[84:85] op_sel_hi:[0,1,1]
	v_pk_fma_f32 v[42:43], v[48:49], v[158:159], v[42:43] op_sel_hi:[0,1,1]
	v_pk_fma_f32 v[84:85], v[48:49], v[214:215], v[114:115] op_sel_hi:[0,1,1]
	v_pk_fma_f32 v[114:115], v[48:49], v[216:217], v[118:119] op_sel_hi:[0,1,1]
	v_pk_fma_f32 v[118:119], v[48:49], v[160:161], v[120:121] op_sel_hi:[0,1,1]
	v_pk_fma_f32 v[120:121], v[48:49], v[218:219], v[130:131] op_sel_hi:[0,1,1]
	v_pk_fma_f32 v[128:129], v[48:49], v[136:137], v[142:143] op_sel_hi:[0,1,1]
	v_pk_fma_f32 v[130:131], v[48:49], v[220:221], v[144:145] op_sel_hi:[0,1,1]
	v_pk_fma_f32 v[122:123], v[48:49], v[162:163], v[122:123] op_sel_hi:[0,1,1]
	v_pk_fma_f32 v[134:135], v[48:49], v[222:223], v[146:147] op_sel_hi:[0,1,1]
	v_pk_fma_f32 v[126:127], v[48:49], v[224:225], v[126:127] op_sel_hi:[0,1,1]
	v_pk_fma_f32 v[132:133], v[48:49], v[138:139], v[132:133] op_sel_hi:[0,1,1]
	v_pk_fma_f32 v[124:125], v[48:49], v[164:165], v[124:125] op_sel_hi:[0,1,1]
	v_pk_fma_f32 v[136:137], v[48:49], v[226:227], v[140:141] op_sel_hi:[0,1,1]
	v_pk_fma_f32 v[138:139], v[48:49], v[228:229], v[148:149] op_sel_hi:[0,1,1]
	v_pk_fma_f32 v[116:117], v[48:49], v[230:231], v[116:117] op_sel_hi:[0,1,1]
	v_pk_fma_f32 v[48:49], v[48:49], v[166:167], v[50:51] op_sel_hi:[0,1,1]
	v_pk_fma_f32 v[42:43], v[52:53], s[12:13], v[42:43] op_sel_hi:[1,0,1]
	v_pk_fma_f32 v[50:51], v[54:55], s[12:13], v[84:85] op_sel_hi:[1,0,1]
	v_pk_fma_f32 v[52:53], v[56:57], s[12:13], v[114:115] op_sel_hi:[1,0,1]
	v_pk_fma_f32 v[54:55], v[58:59], s[12:13], v[118:119] op_sel_hi:[1,0,1]
	v_pk_fma_f32 v[56:57], v[60:61], s[12:13], v[120:121] op_sel_hi:[1,0,1]
	v_pk_fma_f32 v[58:59], v[62:63], s[12:13], v[128:129] op_sel_hi:[1,0,1]
	v_pk_fma_f32 v[60:61], v[64:65], s[12:13], v[130:131] op_sel_hi:[1,0,1]
	v_pk_fma_f32 v[62:63], v[66:67], s[12:13], v[122:123] op_sel_hi:[1,0,1]
	v_pk_fma_f32 v[64:65], v[68:69], s[12:13], v[134:135] op_sel_hi:[1,0,1]
	v_pk_fma_f32 v[66:67], v[70:71], s[12:13], v[126:127] op_sel_hi:[1,0,1]
	v_pk_fma_f32 v[68:69], v[72:73], s[12:13], v[132:133] op_sel_hi:[1,0,1]
	v_pk_fma_f32 v[70:71], v[74:75], s[12:13], v[124:125] op_sel_hi:[1,0,1]
	v_pk_fma_f32 v[72:73], v[76:77], s[12:13], v[136:137] op_sel_hi:[1,0,1]
	v_pk_fma_f32 v[74:75], v[78:79], s[12:13], v[138:139] op_sel_hi:[1,0,1]
	v_pk_fma_f32 v[76:77], v[80:81], s[12:13], v[116:117] op_sel_hi:[1,0,1]
	v_pk_fma_f32 v[48:49], v[82:83], s[12:13], v[48:49] op_sel_hi:[1,0,1]
	s_waitcnt vmcnt(6)
	v_pk_fma_f32 v[18:19], v[42:43], v[90:91], v[18:19]
	v_pk_fma_f32 v[20:21], v[50:51], v[92:93], v[20:21]
	v_pk_fma_f32 v[6:7], v[52:53], v[86:87], v[6:7]
	v_pk_fma_f32 v[8:9], v[54:55], v[88:89], v[8:9]
	s_waitcnt vmcnt(4)
	v_pk_fma_f32 v[10:11], v[56:57], v[98:99], v[10:11]
	v_pk_fma_f32 v[12:13], v[58:59], v[100:101], v[12:13]
	v_pk_fma_f32 v[2:3], v[60:61], v[94:95], v[2:3]
	v_pk_fma_f32 v[4:5], v[62:63], v[96:97], v[4:5]
	s_waitcnt vmcnt(2)
	v_pk_fma_f32 v[30:31], v[64:65], v[38:39], v[30:31]
	v_pk_fma_f32 v[32:33], v[66:67], v[40:41], v[32:33]
	v_pk_fma_f32 v[22:23], v[68:69], v[102:103], v[22:23]
	v_pk_fma_f32 v[24:25], v[70:71], v[104:105], v[24:25]
	s_waitcnt vmcnt(0)
	v_pk_fma_f32 v[26:27], v[72:73], v[110:111], v[26:27]
	v_pk_fma_f32 v[28:29], v[74:75], v[112:113], v[28:29]
	v_pk_fma_f32 v[14:15], v[76:77], v[106:107], v[14:15]
	v_pk_fma_f32 v[16:17], v[48:49], v[108:109], v[16:17]
	global_store_dwordx4 v[44:45], v[18:21], off
	global_store_dwordx4 v[44:45], v[6:9], off offset:16
	global_store_dwordx4 v[44:45], v[10:13], off offset:2048
	global_store_dwordx4 v[44:45], v[2:5], off offset:2064
	global_store_dwordx4 v[46:47], v[30:33], off
	global_store_dwordx4 v[46:47], v[22:25], off offset:16
	global_store_dwordx4 v[46:47], v[26:29], off offset:2048
	global_store_dwordx4 v[46:47], v[14:17], off offset:2064
	s_andn2_b64 exec, exec, s[2:3]
	s_cbranch_execnz .LBB0_1221

; __device__ __forceinline__ int tid_fresh() { int t = threadIdx.x; asm volatile("" : "+v"(t)); return t; }
; template <int MODE>
; __device__ __forceinline__ void combine_phase(LAS unsigned char* ldsb, int bid, int G, const float* x, const float* gf, const bf16_t* Y, const u32x2* rec,
;                                               float* xout, const float* ng, const float* sc, const float* sh, bf16_t* hbuf) {
;     ...
;     for (int rowi = bid * 16 + wave0 * 2; rowi < T; rowi += ((rowi & 1) ? (G * 16 - 1) : 1)) {
;         const int row = rowi;
;         const int lane = tid_fresh() & 63;
;         float a[4][8];
; #pragma unroll
;         for (int i = 0; i < 4; ++i)
; #pragma unroll
;             for (int q = 0; q < 8; ++q) a[i][q] = 0.f;
;         u32x2 rr[TOPK];
; #pragma unroll
;         for (int j = 0; j < TOPK; ++j) rr[j] = rec[row * TOPK + j];
;         float4 xr[4][2];
; #pragma unroll
;         for (int i = 0; i < 4; ++i) { const int c = lane * 8 + i * 512; xr[i][0] = *(const float4*)(x + (size_t)row * D + c); xr[i][1] = *(const float4*)(x + (size_t)row * D + c + 4); }
; #pragma unroll
;         for (int jb = 0; jb <= TOPK; jb += 8) {
;             u32x2 yv[7][4]; float wj[7];
; #pragma unroll
;             for (int jj = 0; jj < 7; ++jj) { const int j = jb + jj; if (j > TOPK) break;
;                 size_t slot = (size_t)SLOT_SH + row; wj[jj] = Y8_INV;
;                 if (j < TOPK) { const int e = (int)(rr[j].x >> 13), pos = (int)(rr[j].x & 8191u); wj[jj] = __uint_as_float(rr[j].y) * Y8_INV; slot = (size_t)tstart[e] * BM + pos; }
;                 const unsigned char* yp = (const unsigned char*)Y + slot * D + lane * 8;
; #pragma unroll
;                 for (int i = 0; i < 4; ++i) yv[jj][i] = *(const u32x2*)(yp + i * 512);
.LBB0_1958:
	v_mul_lo_u32 v2, v66, 6
	v_ashrrev_i32_e32 v3, 31, v2
	v_mov_b32_e32 v4, v0
	v_lshl_add_u64 v[2:3], v[2:3], 3, s[12:13]
	global_load_dwordx4 v[38:41], v[2:3], off
	global_load_dwordx4 v[44:47], v[2:3], off offset:16
	global_load_dwordx4 v[48:51], v[2:3], off offset:32
	v_cmp_lt_i32_e32 vcc, v79, v77
	v_and_b32_e32 v15, 1, v66
	v_ashrrev_i32_e32 v67, 31, v66
	v_cndmask_b32_e32 v5, v1, v79, vcc
	v_cmp_lt_i32_e32 vcc, v113, v77
	v_lshlrev_b64 v[6:7], 13, v[66:67]
	v_lshlrev_b64 v[8:9], 11, v[66:67]
	v_cndmask_b32_e32 v10, v1, v113, vcc
	v_cmp_lt_i32_e32 vcc, v114, v77
	v_lshlrev_b32_e32 v244, 2, v10
	v_mov_b32_e32 v35, v69
	v_cndmask_b32_e32 v11, v1, v114, vcc
	v_cmp_lt_i32_e32 vcc, v115, v77
	v_lshlrev_b32_e32 v245, 2, v11
	v_lshlrev_b32_e32 v11, 3, v4
	v_cndmask_b32_e32 v12, v1, v115, vcc
	v_cmp_lt_i32_e32 vcc, v116, v77
	v_and_b32_e32 v68, 0x1f8, v11
	v_lshl_add_u64 v[52:53], s[10:11], 0, v[68:69]
	v_cndmask_b32_e32 v13, v1, v116, vcc
	v_cmp_lt_i32_e32 vcc, v117, v77
	v_lshlrev_b32_e32 v34, 2, v68
	v_lshl_add_u64 v[2:3], v[52:53], 0, v[8:9]
	v_cndmask_b32_e32 v14, v1, v117, vcc
	v_cmp_eq_u32_e32 vcc, 1, v15
	v_mov_b32_e32 v37, v69
	v_mov_b32_e32 v43, v69
	v_cndmask_b32_e32 v10, 1, v119, vcc
	v_add_u32_e32 v66, v10, v66
	v_cmp_lt_i32_e32 vcc, s16, v66
	v_lshlrev_b32_e32 v67, 2, v5
	v_lshlrev_b32_e32 v248, 2, v14
	v_lshl_add_u64 v[4:5], s[68:69], 0, v[6:7]
	v_lshl_add_u64 v[14:15], s[2:3], 0, v[6:7]
	s_or_b64 s[4:5], vcc, s[4:5]
	v_or_b32_e32 v36, 0x1000, v34
	v_or_b32_e32 v42, 0x1800, v34
	v_add_co_u32_e32 v58, vcc, s14, v2
	v_lshl_add_u64 v[16:17], v[4:5], 0, v[34:35]
	v_lshl_add_u64 v[70:71], v[14:15], 0, v[34:35]
	v_lshl_add_u64 v[54:55], v[4:5], 0, v[36:37]
	v_lshl_add_u64 v[56:57], v[4:5], 0, v[42:43]
	v_addc_co_u32_e32 v59, vcc, 0, v3, vcc
	v_lshl_add_u64 v[74:75], v[14:15], 0, v[36:37]
	v_lshl_add_u64 v[72:73], v[14:15], 0, v[42:43]
	v_lshlrev_b32_e32 v246, 2, v12
	v_lshlrev_b32_e32 v247, 2, v13
	global_load_dwordx4 v[6:9], v[16:17], off offset:16
	global_load_dwordx4 v[18:21], v[16:17], off
	global_load_dwordx4 v[2:5], v[16:17], off offset:2064
	global_load_dwordx4 v[10:13], v[16:17], off offset:2048
	global_load_dwordx2 v[60:61], v[58:59], off nt
	global_load_dwordx2 v[62:63], v[58:59], off offset:512 nt
	global_load_dwordx2 v[64:65], v[58:59], off offset:1024 nt
	global_load_dwordx2 v[110:111], v[58:59], off offset:1536 nt
	global_load_dwordx4 v[22:25], v[54:55], off offset:16
	global_load_dwordx4 v[30:33], v[54:55], off
	global_load_dwordx4 v[14:17], v[56:57], off offset:16
	global_load_dwordx4 v[26:29], v[56:57], off
	v_or_b32_e32 v132, 0x800, v34
	s_waitcnt vmcnt(14)
	v_mul_f32_e32 v152, 0x3d800000, v39
	v_lshrrev_b32_e32 v35, 11, v38
	v_lshlrev_b32_e32 v37, 11, v38
	v_lshrrev_b32_e32 v38, 11, v40
	v_lshlrev_b32_e32 v43, 11, v40
	s_waitcnt vmcnt(13)
	v_lshrrev_b32_e32 v39, 11, v44
	v_lshrrev_b32_e32 v40, 11, v46
	v_mul_f32_e32 v154, 0x3d800000, v41
	v_lshlrev_b32_e32 v54, 11, v44
	s_waitcnt vmcnt(12)
	v_lshrrev_b32_e32 v41, 11, v48
	v_lshrrev_b32_e32 v44, 11, v50
	v_and_b32_e32 v35, 0x1ffffc, v35
	v_and_b32_e32 v68, 0xfff800, v37
	v_and_b32_e32 v37, 0x1ffffc, v38
	v_and_b32_e32 v38, 0x1ffffc, v39
	v_and_b32_e32 v39, 0x1ffffc, v40
	v_and_b32_e32 v40, 0x1ffffc, v41
	v_and_b32_e32 v41, 0x1ffffc, v44
	v_add_u32_e32 v35, s7, v35
	v_add_u32_e32 v44, s7, v38
	v_add_u32_e32 v39, s7, v39
	v_mul_f32_e32 v156, 0x3d800000, v45
	v_lshlrev_b32_e32 v55, 11, v46
	v_lshlrev_b32_e32 v56, 11, v48
	v_lshlrev_b32_e32 v57, 11, v50
	v_add_u32_e32 v37, s7, v37
	v_add_u32_e32 v45, s7, v40
	v_add_u32_e32 v41, s7, v41
	ds_read_b32 v38, v35
	ds_read_b32 v40, v37
	ds_read_b32 v44, v44
	ds_read_b32 v46, v39
	ds_read_b32 v48, v45
	ds_read_b32 v50, v41
	s_waitcnt lgkmcnt(5)
	v_ashrrev_i32_e32 v39, 31, v38
	v_lshlrev_b64 v[38:39], 19, v[38:39]
	v_lshl_add_u64 v[38:39], v[52:53], 0, v[38:39]
	s_waitcnt lgkmcnt(4)
	v_ashrrev_i32_e32 v41, 31, v40
	v_lshl_add_u64 v[38:39], v[38:39], 0, v[68:69]
	v_lshlrev_b64 v[40:41], 19, v[40:41]
	global_load_dwordx2 v[158:159], v[38:39], off nt
	global_load_dwordx2 v[160:161], v[38:39], off offset:512 nt
	global_load_dwordx2 v[162:163], v[38:39], off offset:1024 nt
	global_load_dwordx2 v[164:165], v[38:39], off offset:1536 nt
	v_lshl_add_u64 v[40:41], v[52:53], 0, v[40:41]
	v_and_b32_e32 v68, 0xfff800, v43
	v_lshl_add_u64 v[38:39], v[40:41], 0, v[68:69]
	global_load_dwordx2 v[166:167], v[38:39], off nt
	global_load_dwordx2 v[168:169], v[38:39], off offset:512 nt
	global_load_dwordx2 v[170:171], v[38:39], off offset:1024 nt
	global_load_dwordx2 v[172:173], v[38:39], off offset:1536 nt
	s_waitcnt lgkmcnt(3)
	v_ashrrev_i32_e32 v45, 31, v44
	v_lshlrev_b64 v[44:45], 19, v[44:45]
	v_lshl_add_u64 v[44:45], v[52:53], 0, v[44:45]
	v_and_b32_e32 v68, 0xfff800, v54
	v_lshl_add_u64 v[38:39], v[44:45], 0, v[68:69]
	v_mul_f32_e32 v112, 0x3d800000, v47
	s_waitcnt lgkmcnt(2)
	v_ashrrev_i32_e32 v47, 31, v46
	global_load_dwordx2 v[174:175], v[38:39], off nt
	global_load_dwordx2 v[176:177], v[38:39], off offset:512 nt
	global_load_dwordx2 v[178:179], v[38:39], off offset:1024 nt
	global_load_dwordx2 v[180:181], v[38:39], off offset:1536 nt
	v_lshlrev_b64 v[46:47], 19, v[46:47]
	v_lshl_add_u64 v[46:47], v[52:53], 0, v[46:47]
	v_and_b32_e32 v68, 0xfff800, v55
	v_lshl_add_u64 v[38:39], v[46:47], 0, v[68:69]
	v_mul_f32_e32 v78, 0x3d800000, v49
	s_waitcnt lgkmcnt(1)
	v_ashrrev_i32_e32 v49, 31, v48
	global_load_dwordx2 v[182:183], v[38:39], off nt
	global_load_dwordx2 v[184:185], v[38:39], off offset:512 nt
	global_load_dwordx2 v[186:187], v[38:39], off offset:1024 nt
	global_load_dwordx2 v[188:189], v[38:39], off offset:1536 nt
	v_mul_f32_e32 v76, 0x3d800000, v51
	s_waitcnt lgkmcnt(0)
; template <int MODE>
; __device__ __forceinline__ void combine_phase(LAS unsigned char* ldsb, int bid, int G, const float* x, const float* gf, const bf16_t* Y, const u32x2* rec,
;                                               float* xout, const float* ng, const float* sc, const float* sh, bf16_t* hbuf) {
;     ...
;         for (int i = 0; i < 4; ++i) { const int c = lane * 8 + i * 512; xr[i][0] = *(const float4*)(x + (size_t)row * D + c); xr[i][1] = *(const float4*)(x + (size_t)row * D + c + 4); }
; #pragma unroll
;         for (int jb = 0; jb <= TOPK; jb += 8) {
;             u32x2 yv[7][4]; float wj[7];
; #pragma unroll
;             for (int jj = 0; jj < 7; ++jj) { const int j = jb + jj; if (j > TOPK) break;
;                 size_t slot = (size_t)SLOT_SH + row; wj[jj] = Y8_INV;
;                 if (j < TOPK) { const int e = (int)(rr[j].x >> 13), pos = (int)(rr[j].x & 8191u); wj[jj] = __uint_as_float(rr[j].y) * Y8_INV; slot = (size_t)tstart[e] * BM + pos; }
;                 const unsigned char* yp = (const unsigned char*)Y + slot * D + lane * 8;
; #pragma unroll
;                 for (int i = 0; i < 4; ++i) yv[jj][i] = *(const u32x2*)(yp + i * 512);
;             }
; #pragma unroll
;             for (int jj = 0; jj < 7; ++jj) { const int j = jb + jj; if (j > TOPK) break; const float w = wj[jj];
; #pragma unroll
;                 for (int i = 0; i < 4; ++i) { const u32x2 y2 = yv[jj][i];
;                     const f32x2v p0 = __builtin_amdgcn_cvt_pk_f32_fp8((int)y2.x, false), p1 = __builtin_amdgcn_cvt_pk_f32_fp8((int)y2.x, true), p2 = __builtin_amdgcn_cvt_pk_f32_fp8((int)y2.y, false), p3 = __builtin_amdgcn_cvt_pk_f32_fp8((int)y2.y, true);
;                     a[i][0] += w * p0.x; a[i][1] += w * p0.y; a[i][2] += w * p1.x; a[i][3] += w * p1.y;
;                     a[i][4] += w * p2.x; a[i][5] += w * p2.y; a[i][6] += w * p3.x; a[i][7] += w * p3.y; }
;             }
;             asm volatile("" ::: "memory");
;         }
;         float ss = 0.f;
; #pragma unroll
;         for (int i = 0; i < 4; ++i) { const int c = lane * 8 + i * 512;
; #pragma unroll
;             for (int h = 0; h < 2; ++h) { const float4 xv = xr[i][h], gv = *(const float4*)(gf + c + h * 4);
	v_ashrrev_i32_e32 v51, 31, v50
	v_lshlrev_b64 v[48:49], 19, v[48:49]
	v_lshlrev_b64 v[50:51], 19, v[50:51]
	v_lshl_add_u64 v[48:49], v[52:53], 0, v[48:49]
	v_and_b32_e32 v68, 0xfff800, v56
	v_lshl_add_u64 v[50:51], v[52:53], 0, v[50:51]
	v_lshl_add_u64 v[38:39], v[48:49], 0, v[68:69]
	v_and_b32_e32 v68, 0xfff800, v57
	global_load_dwordx2 v[190:191], v[38:39], off nt
	global_load_dwordx2 v[192:193], v[38:39], off offset:512 nt
	global_load_dwordx2 v[194:195], v[38:39], off offset:1024 nt
	global_load_dwordx2 v[196:197], v[38:39], off offset:1536 nt
	v_lshl_add_u64 v[38:39], v[50:51], 0, v[68:69]
	global_load_dwordx2 v[198:199], v[38:39], off nt
	global_load_dwordx2 v[200:201], v[38:39], off offset:512 nt
	global_load_dwordx2 v[202:203], v[38:39], off offset:1024 nt
	global_load_dwordx2 v[204:205], v[38:39], off offset:1536 nt
	global_load_dwordx4 v[120:123], v34, s[8:9] offset:16
	global_load_dwordx4 v[124:127], v34, s[8:9]
	global_load_dwordx4 v[128:131], v132, s[8:9] offset:16
	s_nop 0
	global_load_dwordx4 v[132:135], v132, s[8:9]
	s_nop 0
	global_load_dwordx4 v[136:139], v36, s[8:9] offset:16
	global_load_dwordx4 v[140:143], v36, s[8:9]
	global_load_dwordx4 v[144:147], v42, s[8:9] offset:16
	global_load_dwordx4 v[148:151], v42, s[8:9]
	s_waitcnt vmcnt(39)
	v_cvt_pk_f32_fp8_e32 v[80:81], v60
	v_cvt_pk_f32_fp8_sdwa v[82:83], v60 src0_sel:WORD_1
	v_cvt_pk_f32_fp8_e32 v[84:85], v61
	v_cvt_pk_f32_fp8_sdwa v[86:87], v61 src0_sel:WORD_1
	s_waitcnt vmcnt(38)
	v_cvt_pk_f32_fp8_e32 v[88:89], v62
	v_cvt_pk_f32_fp8_sdwa v[90:91], v62 src0_sel:WORD_1
	v_cvt_pk_f32_fp8_e32 v[92:93], v63
	v_cvt_pk_f32_fp8_sdwa v[94:95], v63 src0_sel:WORD_1
	s_waitcnt vmcnt(37)
	v_cvt_pk_f32_fp8_e32 v[96:97], v64
	v_cvt_pk_f32_fp8_sdwa v[98:99], v64 src0_sel:WORD_1
	v_cvt_pk_f32_fp8_e32 v[100:101], v65
	v_cvt_pk_f32_fp8_sdwa v[102:103], v65 src0_sel:WORD_1
	global_load_dwordx4 v[54:57], v34, s[0:1] offset:16
	global_load_dwordx4 v[62:65], v34, s[0:1]
	global_load_dwordx4 v[46:49], v34, s[0:1] offset:2064
	global_load_dwordx4 v[58:61], v34, s[0:1] offset:2048
	global_load_dwordx4 v[38:41], v36, s[0:1] offset:16
	global_load_dwordx4 v[50:53], v36, s[0:1]
	s_nop 0
	global_load_dwordx4 v[34:37], v42, s[0:1] offset:16
	s_nop 0
	global_load_dwordx4 v[42:45], v42, s[0:1]
	s_waitcnt vmcnt(44)
	v_cvt_pk_f32_fp8_e32 v[104:105], v110
	v_cvt_pk_f32_fp8_sdwa v[106:107], v110 src0_sel:WORD_1
	v_cvt_pk_f32_fp8_e32 v[108:109], v111
	v_cvt_pk_f32_fp8_sdwa v[110:111], v111 src0_sel:WORD_1
	s_waitcnt vmcnt(39)
	v_cvt_pk_f32_fp8_e32 v[206:207], v158
	v_cvt_pk_f32_fp8_sdwa v[208:209], v158 src0_sel:WORD_1
	v_cvt_pk_f32_fp8_e32 v[210:211], v159
	v_cvt_pk_f32_fp8_sdwa v[158:159], v159 src0_sel:WORD_1
	s_waitcnt vmcnt(38)
	v_cvt_pk_f32_fp8_e32 v[212:213], v160
	v_cvt_pk_f32_fp8_sdwa v[214:215], v160 src0_sel:WORD_1
	v_cvt_pk_f32_fp8_e32 v[216:217], v161
	v_cvt_pk_f32_fp8_sdwa v[160:161], v161 src0_sel:WORD_1
	s_waitcnt vmcnt(37)
	v_cvt_pk_f32_fp8_e32 v[218:219], v162
	v_cvt_pk_f32_fp8_sdwa v[220:221], v162 src0_sel:WORD_1
	v_cvt_pk_f32_fp8_e32 v[222:223], v163
	v_cvt_pk_f32_fp8_sdwa v[162:163], v163 src0_sel:WORD_1
	s_waitcnt vmcnt(36)
	v_cvt_pk_f32_fp8_e32 v[224:225], v164
	v_cvt_pk_f32_fp8_sdwa v[226:227], v164 src0_sel:WORD_1
	v_cvt_pk_f32_fp8_e32 v[228:229], v165
	v_cvt_pk_f32_fp8_sdwa v[164:165], v165 src0_sel:WORD_1
	s_waitcnt vmcnt(35)
	v_cvt_pk_f32_fp8_e32 v[230:231], v166
	v_cvt_pk_f32_fp8_sdwa v[232:233], v166 src0_sel:WORD_1
	s_waitcnt vmcnt(34)
	v_cvt_pk_f32_fp8_e32 v[236:237], v168
	v_pk_fma_f32 v[206:207], v[152:153], v[206:207], 0 op_sel_hi:[0,1,0]
	v_cvt_pk_f32_fp8_e32 v[234:235], v167
	v_cvt_pk_f32_fp8_sdwa v[166:167], v167 src0_sel:WORD_1
	v_cvt_pk_f32_fp8_sdwa v[238:239], v168 src0_sel:WORD_1
	v_cvt_pk_f32_fp8_e32 v[240:241], v169
	v_cvt_pk_f32_fp8_sdwa v[168:169], v169 src0_sel:WORD_1
	v_pk_fma_f32 v[208:209], v[152:153], v[208:209], 0 op_sel_hi:[0,1,0]
	v_pk_fma_f32 v[210:211], v[152:153], v[210:211], 0 op_sel_hi:[0,1,0]
	v_pk_fma_f32 v[158:159], v[152:153], v[158:159], 0 op_sel_hi:[0,1,0]
	v_pk_fma_f32 v[212:213], v[152:153], v[212:213], 0 op_sel_hi:[0,1,0]
	v_pk_fma_f32 v[214:215], v[152:153], v[214:215], 0 op_sel_hi:[0,1,0]
	v_pk_fma_f32 v[216:217], v[152:153], v[216:217], 0 op_sel_hi:[0,1,0]
	v_pk_fma_f32 v[160:161], v[152:153], v[160:161], 0 op_sel_hi:[0,1,0]
	v_pk_fma_f32 v[218:219], v[152:153], v[218:219], 0 op_sel_hi:[0,1,0]
	v_pk_fma_f32 v[220:221], v[152:153], v[220:221], 0 op_sel_hi:[0,1,0]
	v_pk_fma_f32 v[222:223], v[152:153], v[222:223], 0 op_sel_hi:[0,1,0]
	v_pk_fma_f32 v[162:163], v[152:153], v[162:163], 0 op_sel_hi:[0,1,0]
	v_pk_fma_f32 v[224:225], v[152:153], v[224:225], 0 op_sel_hi:[0,1,0]
	v_pk_fma_f32 v[226:227], v[152:153], v[226:227], 0 op_sel_hi:[0,1,0]
	v_pk_fma_f32 v[228:229], v[152:153], v[228:229], 0 op_sel_hi:[0,1,0]
	v_pk_fma_f32 v[152:153], v[152:153], v[164:165], 0 op_sel_hi:[0,1,0]
	s_waitcnt vmcnt(33)
	v_cvt_pk_f32_fp8_e32 v[164:165], v170
	v_pk_fma_f32 v[206:207], v[154:155], v[230:231], v[206:207] op_sel_hi:[0,1,1]
	v_cvt_pk_f32_fp8_sdwa v[230:231], v170 src0_sel:WORD_1
	v_pk_fma_f32 v[208:209], v[154:155], v[232:233], v[208:209] op_sel_hi:[0,1,1]
	v_cvt_pk_f32_fp8_e32 v[232:233], v171
	v_pk_fma_f32 v[212:213], v[154:155], v[236:237], v[212:213] op_sel_hi:[0,1,1]
	s_waitcnt vmcnt(32)
	v_cvt_pk_f32_fp8_e32 v[236:237], v173
	v_cvt_pk_f32_fp8_sdwa v[170:171], v171 src0_sel:WORD_1
	v_pk_fma_f32 v[210:211], v[154:155], v[234:235], v[210:211] op_sel_hi:[0,1,1]
	v_cvt_pk_f32_fp8_e32 v[234:235], v172
	v_pk_fma_f32 v[158:159], v[154:155], v[166:167], v[158:159] op_sel_hi:[0,1,1]
	v_cvt_pk_f32_fp8_sdwa v[166:167], v172 src0_sel:WORD_1
	v_cvt_pk_f32_fp8_sdwa v[172:173], v173 src0_sel:WORD_1
	v_pk_fma_f32 v[214:215], v[154:155], v[238:239], v[214:215] op_sel_hi:[0,1,1]
	s_waitcnt vmcnt(31)
; template <int MODE>
; __device__ __forceinline__ void combine_phase(LAS unsigned char* ldsb, int bid, int G, const float* x, const float* gf, const bf16_t* Y, const u32x2* rec,
;                                               float* xout, const float* ng, const float* sc, const float* sh, bf16_t* hbuf) {
;     ...
;             for (int jj = 0; jj < 7; ++jj) { const int j = jb + jj; if (j > TOPK) break; const float w = wj[jj];
; #pragma unroll
;                 for (int i = 0; i < 4; ++i) { const u32x2 y2 = yv[jj][i];
;                     const f32x2v p0 = __builtin_amdgcn_cvt_pk_f32_fp8((int)y2.x, false), p1 = __builtin_amdgcn_cvt_pk_f32_fp8((int)y2.x, true), p2 = __builtin_amdgcn_cvt_pk_f32_fp8((int)y2.y, false), p3 = __builtin_amdgcn_cvt_pk_f32_fp8((int)y2.y, true);
;                     a[i][0] += w * p0.x; a[i][1] += w * p0.y; a[i][2] += w * p1.x; a[i][3] += w * p1.y;
;                     a[i][4] += w * p2.x; a[i][5] += w * p2.y; a[i][6] += w * p3.x; a[i][7] += w * p3.y; }
;             }
;             asm volatile("" ::: "memory");
;         }
;         float ss = 0.f;
; #pragma unroll
;         for (int i = 0; i < 4; ++i) { const int c = lane * 8 + i * 512;
; #pragma unroll
;             for (int h = 0; h < 2; ++h) { const float4 xv = xr[i][h], gv = *(const float4*)(gf + c + h * 4);
;                 a[i][h * 4 + 0] = xv.x + gv.x * a[i][h * 4 + 0]; a[i][h * 4 + 1] = xv.y + gv.y * a[i][h * 4 + 1]; a[i][h * 4 + 2] = xv.z + gv.z * a[i][h * 4 + 2]; a[i][h * 4 + 3] = xv.w + gv.w * a[i][h * 4 + 3]; }
	v_cvt_pk_f32_fp8_e32 v[238:239], v174
	v_pk_fma_f32 v[216:217], v[154:155], v[240:241], v[216:217] op_sel_hi:[0,1,1]
	v_cvt_pk_f32_fp8_sdwa v[240:241], v174 src0_sel:WORD_1
	v_pk_fma_f32 v[160:161], v[154:155], v[168:169], v[160:161] op_sel_hi:[0,1,1]
	v_cvt_pk_f32_fp8_e32 v[168:169], v175
	v_cvt_pk_f32_fp8_sdwa v[174:175], v175 src0_sel:WORD_1
	v_pk_fma_f32 v[164:165], v[154:155], v[164:165], v[218:219] op_sel_hi:[0,1,1]
	s_waitcnt vmcnt(30)
	v_cvt_pk_f32_fp8_e32 v[218:219], v176
	v_pk_fma_f32 v[220:221], v[154:155], v[230:231], v[220:221] op_sel_hi:[0,1,1]
	v_cvt_pk_f32_fp8_sdwa v[230:231], v176 src0_sel:WORD_1
	v_pk_fma_f32 v[222:223], v[154:155], v[232:233], v[222:223] op_sel_hi:[0,1,1]
	v_cvt_pk_f32_fp8_e32 v[232:233], v177
	v_cvt_pk_f32_fp8_sdwa v[176:177], v177 src0_sel:WORD_1
	v_pk_fma_f32 v[228:229], v[154:155], v[236:237], v[228:229] op_sel_hi:[0,1,1]
	s_waitcnt vmcnt(28)
	v_cvt_pk_f32_fp8_e32 v[236:237], v180
	v_pk_fma_f32 v[162:163], v[154:155], v[170:171], v[162:163] op_sel_hi:[0,1,1]
	v_cvt_pk_f32_fp8_e32 v[170:171], v178
	v_pk_fma_f32 v[224:225], v[154:155], v[234:235], v[224:225] op_sel_hi:[0,1,1]
	v_pk_fma_f32 v[166:167], v[154:155], v[166:167], v[226:227] op_sel_hi:[0,1,1]
	v_pk_fma_f32 v[152:153], v[154:155], v[172:173], v[152:153] op_sel_hi:[0,1,1]
	v_cvt_pk_f32_fp8_sdwa v[154:155], v180 src0_sel:WORD_1
	v_pk_fma_f32 v[158:159], v[156:157], v[174:175], v[158:159] op_sel_hi:[0,1,1]
	s_waitcnt vmcnt(26)
	v_cvt_pk_f32_fp8_e32 v[174:175], v184
	v_pk_fma_f32 v[212:213], v[156:157], v[218:219], v[212:213] op_sel_hi:[0,1,1]
	v_cvt_pk_f32_fp8_sdwa v[218:219], v184 src0_sel:WORD_1
	v_pk_fma_f32 v[214:215], v[156:157], v[230:231], v[214:215] op_sel_hi:[0,1,1]
	v_cvt_pk_f32_fp8_e32 v[230:231], v185
	v_cvt_pk_f32_fp8_sdwa v[184:185], v185 src0_sel:WORD_1
	v_pk_fma_f32 v[216:217], v[156:157], v[232:233], v[216:217] op_sel_hi:[0,1,1]
	s_waitcnt vmcnt(25)
	v_cvt_pk_f32_fp8_e32 v[232:233], v186
	v_cvt_pk_f32_fp8_sdwa v[234:235], v178 src0_sel:WORD_1
	v_cvt_pk_f32_fp8_e32 v[172:173], v181
	v_pk_fma_f32 v[206:207], v[156:157], v[238:239], v[206:207] op_sel_hi:[0,1,1]
	v_cvt_pk_f32_fp8_e32 v[238:239], v182
	v_pk_fma_f32 v[208:209], v[156:157], v[240:241], v[208:209] op_sel_hi:[0,1,1]
	v_cvt_pk_f32_fp8_sdwa v[240:241], v182 src0_sel:WORD_1
	v_pk_fma_f32 v[160:161], v[156:157], v[176:177], v[160:161] op_sel_hi:[0,1,1]
	v_cvt_pk_f32_fp8_sdwa v[176:177], v186 src0_sel:WORD_1
	v_pk_fma_f32 v[224:225], v[156:157], v[236:237], v[224:225] op_sel_hi:[0,1,1]
	s_waitcnt vmcnt(23)
	v_cvt_pk_f32_fp8_e32 v[236:237], v190
	v_pk_fma_f32 v[164:165], v[156:157], v[170:171], v[164:165] op_sel_hi:[0,1,1]
	v_pk_fma_f32 v[154:155], v[156:157], v[154:155], v[166:167] op_sel_hi:[0,1,1]
	v_cvt_pk_f32_fp8_sdwa v[166:167], v190 src0_sel:WORD_1
	v_pk_fma_f32 v[160:161], v[112:113], v[184:185], v[160:161] op_sel_hi:[0,1,1]
	s_waitcnt vmcnt(19)
	v_cvt_pk_f32_fp8_e32 v[184:185], v198
	v_pk_fma_f32 v[168:169], v[156:157], v[168:169], v[210:211] op_sel_hi:[0,1,1]
	v_cvt_pk_f32_fp8_e32 v[210:211], v183
	v_pk_fma_f32 v[164:165], v[112:113], v[232:233], v[164:165] op_sel_hi:[0,1,1]
	v_cvt_pk_f32_fp8_sdwa v[232:233], v198 src0_sel:WORD_1
	v_cvt_pk_f32_fp8_e32 v[226:227], v179
	v_cvt_pk_f32_fp8_sdwa v[178:179], v179 src0_sel:WORD_1
	v_cvt_pk_f32_fp8_sdwa v[180:181], v181 src0_sel:WORD_1
	v_pk_fma_f32 v[220:221], v[156:157], v[234:235], v[220:221] op_sel_hi:[0,1,1]
	v_pk_fma_f32 v[172:173], v[156:157], v[172:173], v[228:229] op_sel_hi:[0,1,1]
	v_cvt_pk_f32_fp8_e32 v[228:229], v191
	v_pk_fma_f32 v[206:207], v[112:113], v[238:239], v[206:207] op_sel_hi:[0,1,1]
	v_cvt_pk_f32_fp8_sdwa v[182:183], v183 src0_sel:WORD_1
	v_cvt_pk_f32_fp8_e32 v[170:171], v187
	v_pk_fma_f32 v[208:209], v[112:113], v[240:241], v[208:209] op_sel_hi:[0,1,1]
	v_pk_fma_f32 v[176:177], v[112:113], v[176:177], v[220:221] op_sel_hi:[0,1,1]
	v_cvt_pk_f32_fp8_e32 v[220:221], v199
	v_pk_fma_f32 v[206:207], v[78:79], v[236:237], v[206:207] op_sel_hi:[0,1,1]
	v_cvt_pk_f32_fp8_sdwa v[190:191], v191 src0_sel:WORD_1
	v_pk_fma_f32 v[166:167], v[78:79], v[166:167], v[208:209] op_sel_hi:[0,1,1]
	v_pk_fma_f32 v[184:185], v[76:77], v[184:185], v[206:207] op_sel_hi:[0,1,1]
	v_cvt_pk_f32_fp8_sdwa v[186:187], v187 src0_sel:WORD_1
	v_pk_fma_f32 v[168:169], v[112:113], v[210:211], v[168:169] op_sel_hi:[0,1,1]
	v_cvt_pk_f32_fp8_sdwa v[198:199], v199 src0_sel:WORD_1
	v_pk_fma_f32 v[166:167], v[76:77], v[232:233], v[166:167] op_sel_hi:[0,1,1]
	v_pk_fma_f32 v[80:81], v[80:81], s[6:7], v[184:185] op_sel_hi:[1,0,1]
	v_pk_fma_f32 v[222:223], v[156:157], v[226:227], v[222:223] op_sel_hi:[0,1,1]
	v_pk_fma_f32 v[162:163], v[156:157], v[178:179], v[162:163] op_sel_hi:[0,1,1]
	v_pk_fma_f32 v[152:153], v[156:157], v[180:181], v[152:153] op_sel_hi:[0,1,1]
	v_cvt_pk_f32_fp8_e32 v[156:157], v192
	v_pk_fma_f32 v[168:169], v[78:79], v[228:229], v[168:169] op_sel_hi:[0,1,1]
	v_pk_fma_f32 v[82:83], v[82:83], s[6:7], v[166:167] op_sel_hi:[1,0,1]
	s_waitcnt vmcnt(14)
; template <int MODE>
; __device__ __forceinline__ void combine_phase(LAS unsigned char* ldsb, int bid, int G, const float* x, const float* gf, const bf16_t* Y, const u32x2* rec,
;                                               float* xout, const float* ng, const float* sc, const float* sh, bf16_t* hbuf) {
;     ...
;             for (int jj = 0; jj < 7; ++jj) { const int j = jb + jj; if (j > TOPK) break; const float w = wj[jj];
; #pragma unroll
;                 for (int i = 0; i < 4; ++i) { const u32x2 y2 = yv[jj][i];
;                     const f32x2v p0 = __builtin_amdgcn_cvt_pk_f32_fp8((int)y2.x, false), p1 = __builtin_amdgcn_cvt_pk_f32_fp8((int)y2.x, true), p2 = __builtin_amdgcn_cvt_pk_f32_fp8((int)y2.y, false), p3 = __builtin_amdgcn_cvt_pk_f32_fp8((int)y2.y, true);
;                     a[i][0] += w * p0.x; a[i][1] += w * p0.y; a[i][2] += w * p1.x; a[i][3] += w * p1.y;
;                     a[i][4] += w * p2.x; a[i][5] += w * p2.y; a[i][6] += w * p3.x; a[i][7] += w * p3.y; }
;             }
;             asm volatile("" ::: "memory");
;         }
;         float ss = 0.f;
; #pragma unroll
;         for (int i = 0; i < 4; ++i) { const int c = lane * 8 + i * 512;
; #pragma unroll
;             for (int h = 0; h < 2; ++h) { const float4 xv = xr[i][h], gv = *(const float4*)(gf + c + h * 4);
;                 a[i][h * 4 + 0] = xv.x + gv.x * a[i][h * 4 + 0]; a[i][h * 4 + 1] = xv.y + gv.y * a[i][h * 4 + 1]; a[i][h * 4 + 2] = xv.z + gv.z * a[i][h * 4 + 2]; a[i][h * 4 + 3] = xv.w + gv.w * a[i][h * 4 + 3]; }
; #pragma unroll
;             for (int q = 0; q < 8; ++q) ss += a[i][q] * a[i][q]; }
	v_pk_fma_f32 v[18:19], v[80:81], v[124:125], v[18:19]
	v_cvt_pk_f32_fp8_e32 v[234:235], v188
	v_pk_fma_f32 v[158:159], v[112:113], v[182:183], v[158:159] op_sel_hi:[0,1,1]
	v_pk_fma_f32 v[170:171], v[112:113], v[170:171], v[222:223] op_sel_hi:[0,1,1]
	v_cvt_pk_f32_fp8_e32 v[222:223], v200
	v_pk_fma_f32 v[168:169], v[76:77], v[220:221], v[168:169] op_sel_hi:[0,1,1]
	v_pk_fma_f32 v[20:21], v[82:83], v[126:127], v[20:21]
	v_pk_mul_f32 v[80:81], v[18:19], v[18:19]
	v_cvt_pk_f32_fp8_sdwa v[180:181], v192 src0_sel:WORD_1
	v_pk_fma_f32 v[158:159], v[78:79], v[190:191], v[158:159] op_sel_hi:[0,1,1]
	v_pk_fma_f32 v[84:85], v[84:85], s[6:7], v[168:169] op_sel_hi:[1,0,1]
	v_pk_mul_f32 v[82:83], v[20:21], v[20:21]
	v_add_f32_e32 v68, v80, v81
	v_pk_fma_f32 v[174:175], v[112:113], v[174:175], v[212:213] op_sel_hi:[0,1,1]
	v_pk_fma_f32 v[162:163], v[112:113], v[186:187], v[162:163] op_sel_hi:[0,1,1]
	v_cvt_pk_f32_fp8_sdwa v[186:187], v200 src0_sel:WORD_1
	v_pk_fma_f32 v[158:159], v[76:77], v[198:199], v[158:159] op_sel_hi:[0,1,1]
	v_pk_fma_f32 v[6:7], v[84:85], v[120:121], v[6:7]
	v_add_f32_e32 v68, v68, v82
	v_cvt_pk_f32_fp8_e32 v[238:239], v193
	v_pk_fma_f32 v[156:157], v[78:79], v[156:157], v[174:175] op_sel_hi:[0,1,1]
	v_pk_fma_f32 v[86:87], v[86:87], s[6:7], v[158:159] op_sel_hi:[1,0,1]
	v_pk_mul_f32 v[84:85], v[6:7], v[6:7]
	v_add_f32_e32 v68, v68, v83
	v_cvt_pk_f32_fp8_sdwa v[226:227], v188 src0_sel:WORD_1
	v_pk_fma_f32 v[214:215], v[112:113], v[218:219], v[214:215] op_sel_hi:[0,1,1]
	v_pk_fma_f32 v[224:225], v[112:113], v[234:235], v[224:225] op_sel_hi:[0,1,1]
	v_cvt_pk_f32_fp8_e32 v[234:235], v201
	v_pk_fma_f32 v[156:157], v[76:77], v[222:223], v[156:157] op_sel_hi:[0,1,1]
	v_pk_fma_f32 v[8:9], v[86:87], v[122:123], v[8:9]
	v_add_f32_e32 v68, v68, v84
	v_cvt_pk_f32_fp8_sdwa v[192:193], v193 src0_sel:WORD_1
	v_pk_fma_f32 v[174:175], v[78:79], v[180:181], v[214:215] op_sel_hi:[0,1,1]
	v_pk_fma_f32 v[88:89], v[88:89], s[6:7], v[156:157] op_sel_hi:[1,0,1]
	v_pk_mul_f32 v[86:87], v[8:9], v[8:9]
	v_add_f32_e32 v68, v68, v85
	v_cvt_pk_f32_fp8_e32 v[178:179], v189
	v_pk_fma_f32 v[216:217], v[112:113], v[230:231], v[216:217] op_sel_hi:[0,1,1]
	v_cvt_pk_f32_fp8_sdwa v[200:201], v201 src0_sel:WORD_1
	v_pk_fma_f32 v[174:175], v[76:77], v[186:187], v[174:175] op_sel_hi:[0,1,1]
	s_waitcnt vmcnt(12)
	v_pk_fma_f32 v[10:11], v[88:89], v[132:133], v[10:11]
	v_add_f32_e32 v68, v68, v86
	v_cvt_pk_f32_fp8_e32 v[240:241], v194
	v_pk_fma_f32 v[180:181], v[78:79], v[238:239], v[216:217] op_sel_hi:[0,1,1]
	v_pk_fma_f32 v[90:91], v[90:91], s[6:7], v[174:175] op_sel_hi:[1,0,1]
	v_pk_mul_f32 v[88:89], v[10:11], v[10:11]
	v_add_f32_e32 v68, v68, v87
	v_cvt_pk_f32_fp8_sdwa v[188:189], v189 src0_sel:WORD_1
	v_pk_fma_f32 v[154:155], v[112:113], v[226:227], v[154:155] op_sel_hi:[0,1,1]
	v_cvt_pk_f32_fp8_e32 v[226:227], v202
	v_pk_fma_f32 v[180:181], v[76:77], v[234:235], v[180:181] op_sel_hi:[0,1,1]
	v_pk_fma_f32 v[12:13], v[90:91], v[134:135], v[12:13]
	v_add_f32_e32 v68, v68, v88
	v_cvt_pk_f32_fp8_sdwa v[210:211], v194 src0_sel:WORD_1
	v_pk_fma_f32 v[160:161], v[78:79], v[192:193], v[160:161] op_sel_hi:[0,1,1]
	v_pk_fma_f32 v[92:93], v[92:93], s[6:7], v[180:181] op_sel_hi:[1,0,1]
	v_pk_mul_f32 v[90:91], v[12:13], v[12:13]
	v_add_f32_e32 v68, v68, v89
	v_pk_fma_f32 v[172:173], v[112:113], v[178:179], v[172:173] op_sel_hi:[0,1,1]
	v_cvt_pk_f32_fp8_sdwa v[178:179], v202 src0_sel:WORD_1
	v_pk_fma_f32 v[160:161], v[76:77], v[200:201], v[160:161] op_sel_hi:[0,1,1]
	v_pk_fma_f32 v[2:3], v[92:93], v[128:129], v[2:3]
	v_add_f32_e32 v68, v68, v90
	v_cvt_pk_f32_fp8_e32 v[182:183], v195
	v_pk_fma_f32 v[164:165], v[78:79], v[240:241], v[164:165] op_sel_hi:[0,1,1]
	v_pk_fma_f32 v[94:95], v[94:95], s[6:7], v[160:161] op_sel_hi:[1,0,1]
	v_pk_mul_f32 v[92:93], v[2:3], v[2:3]
	v_add_f32_e32 v68, v68, v91
	v_pk_fma_f32 v[152:153], v[112:113], v[188:189], v[152:153] op_sel_hi:[0,1,1]
	v_cvt_pk_f32_fp8_e32 v[188:189], v203
	v_pk_fma_f32 v[164:165], v[76:77], v[226:227], v[164:165] op_sel_hi:[0,1,1]
	v_pk_fma_f32 v[4:5], v[94:95], v[130:131], v[4:5]
	v_add_f32_e32 v68, v68, v92
	v_cvt_pk_f32_fp8_sdwa v[194:195], v195 src0_sel:WORD_1
	v_pk_fma_f32 v[176:177], v[78:79], v[210:211], v[176:177] op_sel_hi:[0,1,1]
	v_pk_fma_f32 v[96:97], v[96:97], s[6:7], v[164:165] op_sel_hi:[1,0,1]
	v_pk_mul_f32 v[94:95], v[4:5], v[4:5]
	v_add_f32_e32 v68, v68, v93
	v_cvt_pk_f32_fp8_sdwa v[202:203], v203 src0_sel:WORD_1
	v_pk_fma_f32 v[176:177], v[76:77], v[178:179], v[176:177] op_sel_hi:[0,1,1]
	s_waitcnt vmcnt(10)
; __device__ __forceinline__ unsigned cvt_pk_bf16(float lo, float hi) { unsigned r; asm volatile("v_cvt_pk_bf16_f32 %0, %1, %2" : "=v"(r) : "v"(lo), "v"(hi)); return r; }
; template <int MODE>
; __device__ __forceinline__ void combine_phase(LAS unsigned char* ldsb, int bid, int G, const float* x, const float* gf, const bf16_t* Y, const u32x2* rec,
;                                               float* xout, const float* ng, const float* sc, const float* sh, bf16_t* hbuf) {
;     ...
;             for (int q = 0; q < 8; ++q) ss += a[i][q] * a[i][q]; }
;         if (MODE == 0 || MODE == 2) {
; #pragma unroll
;             for (int i = 0; i < 4; ++i) { float* op = xout + (size_t)row * D + lane * 8 + i * 512; *(float4*)op = make_float4(a[i][0], a[i][1], a[i][2], a[i][3]); *(float4*)(op + 4) = make_float4(a[i][4], a[i][5], a[i][6], a[i][7]); }
;         }
;         if (MODE == 1 || MODE == 2) {
;             ss = wave_sum(ss);
;             const float r = rsqrtf(ss * (1.f / D) + EPS);
;             asm volatile("" ::: "memory");
;             float4 g4[4][2];
; #pragma unroll
;             for (int i = 0; i < 4; ++i) { const int c = lane * 8 + i * 512; g4[i][0] = *(const float4*)(ng + c); g4[i][1] = *(const float4*)(ng + c + 4); }
; #pragma unroll
;             for (int i = 0; i < 4; ++i) { const int c = lane * 8 + i * 512; float o[8];
;                 const float gq[8] = {g4[i][0].x, g4[i][0].y, g4[i][0].z, g4[i][0].w, g4[i][1].x, g4[i][1].y, g4[i][1].z, g4[i][1].w};
; #pragma unroll
;                 for (int q = 0; q < 8; ++q) { o[q] = a[i][q] * r * gq[q]; if (MODE == 2) o[q] = o[q] * (1.f + sc[c + q]) + sh[c + q]; }
;                 if (MODE == 1) { float* op = xout + (size_t)row * D + c; *(float4*)op = make_float4(o[0], o[1], o[2], o[3]); *(float4*)(op + 4) = make_float4(o[4], o[5], o[6], o[7]); }
;                 else { u32x4 w; w.x = cvt_pk_bf16(o[0], o[1]); w.y = cvt_pk_bf16(o[2], o[3]); w.z = cvt_pk_bf16(o[4], o[5]); w.w = cvt_pk_bf16(o[6], o[7]); *(u32x4*)(hbuf + (size_t)row * D + c) = w; } }
	v_pk_fma_f32 v[30:31], v[96:97], v[140:141], v[30:31]
	v_add_f32_e32 v68, v68, v94
	v_cvt_pk_f32_fp8_e32 v[212:213], v196
	v_pk_fma_f32 v[170:171], v[78:79], v[182:183], v[170:171] op_sel_hi:[0,1,1]
	v_pk_fma_f32 v[98:99], v[98:99], s[6:7], v[176:177] op_sel_hi:[1,0,1]
	v_pk_mul_f32 v[96:97], v[30:31], v[30:31]
	v_add_f32_e32 v68, v68, v95
	v_cvt_pk_f32_fp8_e32 v[242:243], v204
	v_pk_fma_f32 v[170:171], v[76:77], v[188:189], v[170:171] op_sel_hi:[0,1,1]
	v_pk_fma_f32 v[32:33], v[98:99], v[142:143], v[32:33]
	v_add_f32_e32 v68, v68, v96
	v_cvt_pk_f32_fp8_sdwa v[218:219], v196 src0_sel:WORD_1
	v_pk_fma_f32 v[162:163], v[78:79], v[194:195], v[162:163] op_sel_hi:[0,1,1]
	v_pk_fma_f32 v[100:101], v[100:101], s[6:7], v[170:171] op_sel_hi:[1,0,1]
	v_pk_mul_f32 v[98:99], v[32:33], v[32:33]
	v_add_f32_e32 v68, v68, v97
	v_cvt_pk_f32_fp8_sdwa v[236:237], v204 src0_sel:WORD_1
	v_pk_fma_f32 v[162:163], v[76:77], v[202:203], v[162:163] op_sel_hi:[0,1,1]
	v_pk_fma_f32 v[22:23], v[100:101], v[136:137], v[22:23]
	v_add_f32_e32 v68, v68, v98
	v_cvt_pk_f32_fp8_e32 v[230:231], v197
	v_pk_fma_f32 v[182:183], v[78:79], v[212:213], v[224:225] op_sel_hi:[0,1,1]
	v_pk_fma_f32 v[102:103], v[102:103], s[6:7], v[162:163] op_sel_hi:[1,0,1]
	v_pk_mul_f32 v[100:101], v[22:23], v[22:23]
	v_add_f32_e32 v68, v68, v99
	v_cvt_pk_f32_fp8_e32 v[208:209], v205
	v_pk_fma_f32 v[178:179], v[76:77], v[242:243], v[182:183] op_sel_hi:[0,1,1]
	v_pk_fma_f32 v[24:25], v[102:103], v[138:139], v[24:25]
	v_add_f32_e32 v68, v68, v100
	v_cvt_pk_f32_fp8_sdwa v[196:197], v197 src0_sel:WORD_1
	v_pk_fma_f32 v[154:155], v[78:79], v[218:219], v[154:155] op_sel_hi:[0,1,1]
	v_pk_fma_f32 v[104:105], v[104:105], s[6:7], v[178:179] op_sel_hi:[1,0,1]
	v_pk_mul_f32 v[102:103], v[24:25], v[24:25]
	v_add_f32_e32 v68, v68, v101
	v_cvt_pk_f32_fp8_sdwa v[204:205], v205 src0_sel:WORD_1
	v_pk_fma_f32 v[154:155], v[76:77], v[236:237], v[154:155] op_sel_hi:[0,1,1]
	s_waitcnt vmcnt(8)
	v_pk_fma_f32 v[26:27], v[104:105], v[148:149], v[26:27]
	v_add_f32_e32 v68, v68, v102
	v_pk_fma_f32 v[172:173], v[78:79], v[230:231], v[172:173] op_sel_hi:[0,1,1]
	v_pk_fma_f32 v[106:107], v[106:107], s[6:7], v[154:155] op_sel_hi:[1,0,1]
	v_pk_mul_f32 v[104:105], v[26:27], v[26:27]
	v_add_f32_e32 v68, v68, v103
	v_pk_fma_f32 v[172:173], v[76:77], v[208:209], v[172:173] op_sel_hi:[0,1,1]
	v_pk_fma_f32 v[28:29], v[106:107], v[150:151], v[28:29]
	v_add_f32_e32 v68, v68, v104
	v_pk_fma_f32 v[152:153], v[78:79], v[196:197], v[152:153] op_sel_hi:[0,1,1]
	v_pk_fma_f32 v[108:109], v[108:109], s[6:7], v[172:173] op_sel_hi:[1,0,1]
	v_pk_mul_f32 v[106:107], v[28:29], v[28:29]
	v_add_f32_e32 v68, v68, v105
	v_pk_fma_f32 v[152:153], v[76:77], v[204:205], v[152:153] op_sel_hi:[0,1,1]
	v_pk_fma_f32 v[14:15], v[108:109], v[144:145], v[14:15]
	v_add_f32_e32 v68, v68, v106
	v_pk_fma_f32 v[110:111], v[110:111], s[6:7], v[152:153] op_sel_hi:[1,0,1]
	v_pk_mul_f32 v[108:109], v[14:15], v[14:15]
	v_add_f32_e32 v68, v68, v107
	v_pk_fma_f32 v[16:17], v[110:111], v[146:147], v[16:17]
	v_add_f32_e32 v68, v68, v108
	v_pk_mul_f32 v[110:111], v[16:17], v[16:17]
	v_add_f32_e32 v68, v68, v109
	v_add_f32_e32 v68, v68, v110
	v_add_f32_e32 v68, v68, v111
	ds_bpermute_b32 v67, v67, v68
	s_waitcnt lgkmcnt(0)
	v_add_f32_e32 v67, v68, v67
	ds_bpermute_b32 v68, v244, v67
	s_waitcnt lgkmcnt(0)
	v_add_f32_e32 v67, v67, v68
	ds_bpermute_b32 v68, v245, v67
	s_waitcnt lgkmcnt(0)
	v_add_f32_e32 v67, v67, v68
	ds_bpermute_b32 v68, v246, v67
	s_waitcnt lgkmcnt(0)
	v_add_f32_e32 v67, v67, v68
	ds_bpermute_b32 v68, v247, v67
	s_waitcnt lgkmcnt(0)
	v_add_f32_e32 v67, v67, v68
	ds_bpermute_b32 v68, v248, v67
	s_waitcnt lgkmcnt(0)
	v_add_f32_e32 v67, v67, v68
	v_fmamk_f32 v67, v67, 0x3a000000, v118
	v_mul_f32_e32 v68, 0x4b800000, v67
	v_cmp_gt_f32_e32 vcc, s15, v67
	s_nop 1
	v_cndmask_b32_e32 v67, v67, v68, vcc
	v_rsq_f32_e32 v67, v67
	s_nop 0
	v_mul_f32_e32 v68, 0x45800000, v67
	v_cndmask_b32_e32 v68, v67, v68, vcc
	v_pk_mul_f32 v[18:19], v[18:19], v[68:69] op_sel_hi:[1,0]
	v_pk_mul_f32 v[20:21], v[20:21], v[68:69] op_sel_hi:[1,0]
	v_pk_mul_f32 v[6:7], v[6:7], v[68:69] op_sel_hi:[1,0]
	v_pk_mul_f32 v[8:9], v[8:9], v[68:69] op_sel_hi:[1,0]
	v_pk_mul_f32 v[10:11], v[10:11], v[68:69] op_sel_hi:[1,0]
	v_pk_mul_f32 v[12:13], v[12:13], v[68:69] op_sel_hi:[1,0]
	v_pk_mul_f32 v[80:81], v[2:3], v[68:69] op_sel_hi:[1,0]
	v_pk_mul_f32 v[82:83], v[4:5], v[68:69] op_sel_hi:[1,0]
	v_pk_mul_f32 v[30:31], v[30:31], v[68:69] op_sel_hi:[1,0]
	v_pk_mul_f32 v[32:33], v[32:33], v[68:69] op_sel_hi:[1,0]
	v_pk_mul_f32 v[22:23], v[22:23], v[68:69] op_sel_hi:[1,0]
	v_pk_mul_f32 v[24:25], v[24:25], v[68:69] op_sel_hi:[1,0]
	v_pk_mul_f32 v[26:27], v[26:27], v[68:69] op_sel_hi:[1,0]
	v_pk_mul_f32 v[28:29], v[28:29], v[68:69] op_sel_hi:[1,0]
	v_pk_mul_f32 v[84:85], v[14:15], v[68:69] op_sel_hi:[1,0]
	v_pk_mul_f32 v[86:87], v[16:17], v[68:69] op_sel_hi:[1,0]
	s_waitcnt vmcnt(6)
	v_pk_mul_f32 v[2:3], v[62:63], v[18:19]
	v_pk_mul_f32 v[4:5], v[64:65], v[20:21]
	v_pk_mul_f32 v[6:7], v[54:55], v[6:7]
	v_pk_mul_f32 v[8:9], v[56:57], v[8:9]
	s_waitcnt vmcnt(4)
	v_pk_mul_f32 v[10:11], v[58:59], v[10:11]
	v_pk_mul_f32 v[12:13], v[12:13], v[60:61]
	v_pk_mul_f32 v[14:15], v[80:81], v[46:47]
	v_pk_mul_f32 v[16:17], v[82:83], v[48:49]
	s_waitcnt vmcnt(2)
	v_pk_mul_f32 v[18:19], v[30:31], v[50:51]
	v_pk_mul_f32 v[20:21], v[32:33], v[52:53]
	v_pk_mul_f32 v[22:23], v[22:23], v[38:39]
	v_pk_mul_f32 v[24:25], v[24:25], v[40:41]
	s_waitcnt vmcnt(0)
	v_pk_mul_f32 v[26:27], v[26:27], v[42:43]
	v_pk_mul_f32 v[28:29], v[28:29], v[44:45]
	v_pk_mul_f32 v[30:31], v[84:85], v[34:35]
	v_pk_mul_f32 v[32:33], v[86:87], v[36:37]
	global_store_dwordx4 v[70:71], v[2:5], off
	global_store_dwordx4 v[70:71], v[6:9], off offset:16
	global_store_dwordx4 v[70:71], v[10:13], off offset:2048
	global_store_dwordx4 v[70:71], v[14:17], off offset:2064
	global_store_dwordx4 v[74:75], v[18:21], off
	global_store_dwordx4 v[74:75], v[22:25], off offset:16
	global_store_dwordx4 v[72:73], v[26:29], off
	global_store_dwordx4 v[72:73], v[30:33], off offset:16
	s_andn2_b64 exec, exec, s[4:5]
	s_cbranch_execnz .LBB0_1958
